# V image rows stored with the 16-byte chunks XOR-swizzled by row (as the K image), transposed-read addresses swizzled to match: no 8-way LDS bank conflict in the PV loop
# speedup vs baseline: 1.0038x; 1.0038x over previous
.LBB0_427:
	v_or_b32_e32 v3, s3, v7
	v_lshlrev_b32_e32 v3, s1, v3
	v_add_u32_e32 v180, s42, v3
	s_movk_i32 s4, 0x1880
	v_mov_b64_e32 v[10:11], s[84:85]
	v_mad_i64_i32 v[10:11], s[4:5], v180, s4, v[10:11]
	s_lshl_b32 s4, s2, 1
	s_mov_b32 s5, 0
	v_lshl_add_u64 v[10:11], v[10:11], 0, s[4:5]
	v_lshlrev_b32_e32 v12, 4, v6
	v_mov_b32_e32 v13, 0
	v_lshl_add_u64 v[10:11], v[10:11], 0, v[12:13]
	global_load_dwordx4 v[146:149], v[10:11], off offset:96
	global_load_dwordx4 v[150:153], v[10:11], off offset:64
	global_load_dwordx4 v[154:157], v[10:11], off offset:32
	global_load_dwordx4 v[158:161], v[10:11], off
	s_lshl_b32 s81, 1, s1
	s_lshl_b32 s1, 0xffffff80, s1
	s_waitcnt vmcnt(0)
	s_add_i32 s82, s42, s1
	v_lshlrev_b32_e32 v2, 4, v2
	s_movk_i32 s1, 0x1000
	v_add3_u32 v182, v1, v2, s1
	s_movk_i32 s16, 0x1880
	v_and_b32_e32 v100, 63, v0
	v_lshrrev_b32_e32 v101, 3, v100
	v_and_b32_e32 v104, 7, v100
	v_xor_b32_e32 v104, v104, v101
	v_lshlrev_b32_e32 v104, 4, v104
	s_lshl_b32 s10, s88, 7
	s_add_u32 s10, s10, 0x800
	v_add_u32_e32 v104, s10, v104
	s_bfe_u32 s11, s75, 0x2000c
	s_and_b32 s12, s75, 0xffff0000
	s_add_u32 s12, s12, 0x8000
	s_add_u32 s13, s11, 1
	s_lshl_b32 s10, s13, 5
	v_add_u32_e32 v102, s10, v101
	v_mul_u32_u24_e32 v103, s81, v102
	v_add_u32_e32 v103, s82, v103
	s_lshl_b32 s10, s13, 12
	s_add_u32 s10, s10, s12
	s_lshl_b32 s13, s81, 3
	v_max_i32_e32 v106, 0, v103
	s_mov_b32 m0, s10
	v_mad_u32_u24 v108, v106, s16, v104
	global_load_lds_dwordx4 v108, s[84:85]
	v_add_u32_e32 v103, s13, v103
	v_max_i32_e32 v106, 0, v103
	s_add_u32 m0, s10, 0x400
	v_mad_u32_u24 v108, v106, s16, v104
	global_load_lds_dwordx4 v108, s[84:85]
	v_add_u32_e32 v103, s13, v103
	v_max_i32_e32 v106, 0, v103
	s_add_u32 m0, s10, 0x800
	v_mad_u32_u24 v108, v106, s16, v104
	global_load_lds_dwordx4 v108, s[84:85]
	v_add_u32_e32 v103, s13, v103
	v_max_i32_e32 v106, 0, v103
	s_add_u32 m0, s10, 0xc00
	v_mad_u32_u24 v108, v106, s16, v104
	global_load_lds_dwordx4 v108, s[84:85]
	s_add_u32 s13, s11, 4
	s_cmp_eq_u32 s11, 0
	s_cselect_b32 s13, 0, s13
	s_lshl_b32 s10, s13, 5
	v_add_u32_e32 v102, s10, v101
	v_mul_u32_u24_e32 v103, s81, v102
	v_add_u32_e32 v103, s82, v103
	s_lshl_b32 s10, s13, 12
	s_add_u32 s10, s10, s12
	s_lshl_b32 s13, s81, 3
	v_max_i32_e32 v106, 0, v103
	s_mov_b32 m0, s10
	v_mad_u32_u24 v108, v106, s16, v104
	global_load_lds_dwordx4 v108, s[84:85]
	v_add_u32_e32 v103, s13, v103
	v_max_i32_e32 v106, 0, v103
	s_add_u32 m0, s10, 0x400
	v_mad_u32_u24 v108, v106, s16, v104
	global_load_lds_dwordx4 v108, s[84:85]
	v_add_u32_e32 v103, s13, v103
	v_max_i32_e32 v106, 0, v103
	s_add_u32 m0, s10, 0x800
	v_mad_u32_u24 v108, v106, s16, v104
	global_load_lds_dwordx4 v108, s[84:85]
	v_add_u32_e32 v103, s13, v103
	v_max_i32_e32 v106, 0, v103
	s_add_u32 m0, s10, 0xc00
	v_mad_u32_u24 v108, v106, s16, v104
	global_load_lds_dwordx4 v108, s[84:85]
	v_and_b32_e32 v100, 63, v0
	v_lshrrev_b32_e32 v101, 3, v100
	v_and_b32_e32 v104, 7, v100
	v_xor_b32_e32 v104, v104, v101
	v_lshlrev_b32_e32 v104, 4, v104
	s_lshl_b32 s10, s88, 7
	s_add_u32 s10, s10, 0x1000
	v_add_u32_e32 v104, s10, v104
	s_bfe_u32 s11, s75, 0x2000c
	s_and_b32 s12, s75, 0xffff0000
	s_add_u32 s13, s11, 1
	s_lshl_b32 s10, s13, 5
	v_add_u32_e32 v102, s10, v101
	v_mul_u32_u24_e32 v103, s81, v102
	v_add_u32_e32 v103, s82, v103
	s_lshl_b32 s10, s13, 12
	s_add_u32 s10, s10, s12
	s_lshl_b32 s13, s81, 3
	v_max_i32_e32 v106, 0, v103
	s_mov_b32 m0, s10
	v_mad_u32_u24 v108, v106, s16, v104
	global_load_lds_dwordx4 v108, s[84:85]
	v_add_u32_e32 v103, s13, v103
	v_max_i32_e32 v106, 0, v103
	s_add_u32 m0, s10, 0x400
	v_mad_u32_u24 v108, v106, s16, v104
	global_load_lds_dwordx4 v108, s[84:85]
	v_add_u32_e32 v103, s13, v103
	v_max_i32_e32 v106, 0, v103
	s_add_u32 m0, s10, 0x800
	v_mad_u32_u24 v108, v106, s16, v104
	global_load_lds_dwordx4 v108, s[84:85]
	v_add_u32_e32 v103, s13, v103
	v_max_i32_e32 v106, 0, v103
	s_add_u32 m0, s10, 0xc00
	v_mad_u32_u24 v108, v106, s16, v104
	global_load_lds_dwordx4 v108, s[84:85]
	s_add_u32 s13, s11, 4
	s_cmp_eq_u32 s11, 0
	s_cselect_b32 s13, 0, s13
	s_lshl_b32 s10, s13, 5
	v_add_u32_e32 v102, s10, v101
	v_mul_u32_u24_e32 v103, s81, v102
	v_add_u32_e32 v103, s82, v103
	s_lshl_b32 s10, s13, 12
	s_add_u32 s10, s10, s12
	s_lshl_b32 s13, s81, 3
	v_max_i32_e32 v106, 0, v103
	s_mov_b32 m0, s10
	v_mad_u32_u24 v108, v106, s16, v104
	global_load_lds_dwordx4 v108, s[84:85]
	v_add_u32_e32 v103, s13, v103
	v_max_i32_e32 v106, 0, v103
	s_add_u32 m0, s10, 0x400
	v_mad_u32_u24 v108, v106, s16, v104
	global_load_lds_dwordx4 v108, s[84:85]
	v_add_u32_e32 v103, s13, v103
	v_max_i32_e32 v106, 0, v103
	s_add_u32 m0, s10, 0x800
	v_mad_u32_u24 v108, v106, s16, v104
	global_load_lds_dwordx4 v108, s[84:85]
	v_add_u32_e32 v103, s13, v103
	v_max_i32_e32 v106, 0, v103
	s_add_u32 m0, s10, 0xc00
	v_mad_u32_u24 v108, v106, s16, v104
	global_load_lds_dwordx4 v108, s[84:85]
	s_waitcnt vmcnt(0)
	s_barrier
	s_andn2_b64 vcc, exec, s[8:9]
	s_cbranch_vccz .LBB0_429
	s_branch .LBB0_492

.LBB0_429:
	v_writelane_b32 v254, s78, 15
	s_add_u32 s1, s6, 0x1400000
	s_mov_b32 s2, s90
	v_writelane_b32 v254, s79, 16
	v_writelane_b32 v254, s1, 17
	s_addc_u32 s1, s7, 0
	v_writelane_b32 v254, s1, 18
	v_lshlrev_b32_e32 v10, 1, v4
	v_writelane_b32 v254, s2, 19
	v_and_b32_e32 v10, 32, v10
	v_lshlrev_b32_e32 v11, 3, v4
	v_writelane_b32 v254, s3, 20
	s_add_i32 s1, s3, 32
	v_mov_b32_e32 v179, 0
	v_and_or_b32 v13, v11, 24, v10
	v_lshlrev_b32_e32 v10, 4, v4
	v_writelane_b32 v254, s1, 21
	s_or_b32 s1, s21, 0xffffff80
	v_and_b32_e32 v10, 0x70, v10
	v_mov_b32_e32 v11, v179
	v_writelane_b32 v254, s1, 22
	v_or_b32_e32 v192, s1, v5
	s_add_i32 s1, s3, 0xffffffa0
	v_lshl_add_u64 v[10:11], s[6:7], 0, v[10:11]
	s_mov_b64 s[4:5], 0x12000000
	v_writelane_b32 v254, s1, 23
	v_lshl_add_u64 v[184:185], v[10:11], 0, s[4:5]
	s_or_b32 s4, s3, 8
	v_writelane_b32 v254, s4, 24
	s_or_b32 s4, s3, 16
	v_writelane_b32 v254, s4, 25
	s_or_b32 s4, s3, 24
	v_writelane_b32 v254, s4, 26
	s_add_i32 s4, s3, 40
	v_writelane_b32 v254, s4, 27
	s_add_i32 s4, s3, 48
	v_writelane_b32 v254, s4, 28
	s_add_i32 s4, s3, 56
	v_writelane_b32 v254, s4, 29
	s_or_b32 s4, s21, 0xffffff88
	v_writelane_b32 v254, s4, 30
	s_or_b32 s4, s21, 0xffffff90
	v_writelane_b32 v254, s4, 31
	s_or_b32 s4, s21, 0xffffff98
	v_writelane_b32 v254, s4, 32
	s_add_i32 s4, s3, 0xffffffa8
	v_writelane_b32 v254, s4, 33
	s_add_i32 s4, s3, 0xffffffb0
	v_lshlrev_b32_e32 v12, 2, v6
	v_writelane_b32 v254, s4, 34
	s_add_i32 s4, s3, 0xffffffb8
	v_writelane_b32 v254, s4, 35
	v_cmp_gt_u32_e64 s[4:5], v12, v7
	v_or_b32_e32 v15, 1, v12
	v_cmp_lt_u32_e64 s[8:9], v12, v7
	v_writelane_b32 v254, s4, 36
	v_and_b32_e32 v3, 7, v4
	v_lshlrev_b32_e32 v193, 4, v3
	v_writelane_b32 v254, s5, 37
	v_cmp_lt_u32_e64 s[4:5], v15, v7
	v_or_b32_e32 v15, 2, v12
	v_lshlrev_b32_e32 v2, 3, v6
	v_writelane_b32 v254, s4, 38
	v_cmp_gt_u32_e64 s[6:7], 32, v8
	v_bitop3_b32 v8, v6, v4, 7 bitop3:0x78
	v_writelane_b32 v254, s5, 39
	v_cmp_lt_u32_e64 s[4:5], v15, v7
	v_bitop3_b32 v10, v6, v3, 2 bitop3:0x36
	v_bitop3_b32 v11, v6, v3, 4 bitop3:0x36
	v_writelane_b32 v254, s4, 40
	v_bitop3_b32 v3, v6, v3, 6 bitop3:0x36
	s_add_i32 s83, s75, 0x1000
	v_writelane_b32 v254, s5, 41
	v_cmp_gt_u32_e64 s[4:5], v15, v7
	v_or_b32_e32 v15, 3, v12
	v_or_b32_e32 v1, s3, v7
	v_writelane_b32 v254, s4, 42
	v_bitop3_b32 v9, v5, v4, 7 bitop3:0x78
	v_lshl_add_u32 v14, v7, 7, s75
	v_writelane_b32 v254, s5, 43
	v_cmp_lt_u32_e64 s[4:5], v15, v7
	v_or_b32_e32 v19, 8, v5
	s_lshl_b32 s22, s90, 2
	v_writelane_b32 v254, s4, 44
	v_lshl_add_u32 v18, v5, 7, s75
	v_or_b32_e32 v203, s3, v5
	v_writelane_b32 v254, s5, 45
	v_cmp_gt_u32_e64 s[4:5], v15, v7
	v_or_b32_e32 v15, 8, v12
	v_lshl_add_u32 v20, v19, 7, s75
	v_writelane_b32 v254, s4, 46
	v_or_b32_e32 v204, s3, v19
	v_or_b32_e32 v19, 16, v5
	v_writelane_b32 v254, s5, 47
	v_cmp_lt_u32_e64 s[4:5], v15, v7
	v_add_u32_e32 v194, v14, v2
	v_lshlrev_b32_e32 v8, 4, v8
	v_writelane_b32 v254, s4, 48
	v_lshlrev_b32_e32 v10, 4, v10
	v_lshlrev_b32_e32 v11, 4, v11
	v_writelane_b32 v254, s5, 49
	v_cmp_gt_u32_e64 s[4:5], v15, v7
	v_or_b32_e32 v15, 9, v12
	v_lshlrev_b32_e32 v3, 4, v3
	v_writelane_b32 v254, s4, 50
	v_xor_b32_e32 v16, 0x60, v193
	v_xor_b32_e32 v17, 0x70, v193
	v_writelane_b32 v254, s5, 51
	v_cmp_lt_u32_e64 s[4:5], v15, v7
	v_lshl_add_u32 v21, v19, 7, s75
	v_or_b32_e32 v205, s3, v19
	v_writelane_b32 v254, s4, 52
	v_lshlrev_b32_e32 v186, 1, v2
	v_mbcnt_lo_u32_b32 v2, -1, 0
	v_writelane_b32 v254, s5, 53
	v_cmp_gt_u32_e64 s[4:5], v15, v7
	v_or_b32_e32 v15, 10, v12
	s_xor_b32 s1, s3, 0x7f
	v_writelane_b32 v254, s4, 54
	s_add_i32 s2, s3, 64
	s_add_i32 s10, s3, 0x48
	v_writelane_b32 v254, s5, 55
	v_cmp_lt_u32_e64 s[4:5], v15, v7
	s_add_i32 s11, s3, 0x50
	s_add_i32 s12, s3, 0x58
	v_writelane_b32 v254, s4, 56
	s_add_i32 s13, s3, 0x60
	s_add_i32 s14, s3, 0x68
	v_writelane_b32 v254, s5, 57
	v_cmp_gt_u32_e64 s[4:5], v15, v7
	v_or_b32_e32 v15, 11, v12
	s_add_i32 s15, s3, 0x70
	v_writelane_b32 v254, s4, 58
	s_add_i32 s16, s3, 0x78
	s_or_b32 s17, s3, 0x80
	v_writelane_b32 v254, s5, 59
	v_cmp_lt_u32_e64 s[4:5], v15, v7
	s_or_b32 s18, s3, 0x88
	s_or_b32 s19, s3, 0x90
	v_writelane_b32 v254, s4, 60
	s_or_b32 s20, s3, 0x98
	v_or_b32_e32 v208, 0x1000, v193
	v_writelane_b32 v254, s5, 61
	v_cmp_gt_u32_e64 s[4:5], v15, v7
	v_or_b32_e32 v15, 16, v12
	s_mov_b32 s91, 0
	v_writelane_b32 v254, s4, 62
	s_movk_i32 s21, 0x1880
	s_mov_b64 s[92:93], 0x800
	v_writelane_b32 v254, s5, 63
	v_cmp_lt_u32_e64 s[4:5], v15, v7
	s_add_i32 s23, s75, 0x2400
	s_add_i32 s24, s75, 0x1000
	v_writelane_b32 v255, s4, 0
	s_add_i32 s25, s75, 0x2c00
	s_mov_b64 s[94:95], 0x1000
	v_writelane_b32 v255, s5, 1
	v_cmp_gt_u32_e64 s[4:5], v15, v7
	v_or_b32_e32 v15, 17, v12
	s_cmp_eq_u32 s3, 0
	s_cselect_b32 s26, 0, 0x4000
	s_add_i32 s26, s26, s75
	v_writelane_b32 v255, s4, 2
	s_add_i32 s27, s75, 0xc00
	s_add_i32 s28, s75, 0x1400
	v_writelane_b32 v255, s5, 3
	v_cmp_lt_u32_e64 s[4:5], v15, v7
	s_add_i32 s29, s75, 0x1800
	s_add_i32 s30, s75, 0x1c00
	v_writelane_b32 v255, s4, 4
	s_add_i32 s31, s75, 0x3000
	s_add_i32 s34, s75, 0x3400
	v_writelane_b32 v255, s5, 5
	v_cmp_gt_u32_e64 s[4:5], v15, v7
	v_or_b32_e32 v15, 18, v12
	s_add_i32 s35, s75, 0x3800
	v_writelane_b32 v255, s4, 6
	s_add_i32 s36, s75, 0x3c00
	v_mbcnt_hi_u32_b32 v209, -1, v2
	v_writelane_b32 v255, s5, 7
	v_cmp_lt_u32_e64 s[4:5], v15, v7
	v_add_u32_e32 v215, v194, v16
	v_add_u32_e32 v216, v194, v17
	v_writelane_b32 v255, s4, 8
	v_add_u32_e32 v221, v14, v8
	v_add_u32_e32 v222, v14, v10
	v_writelane_b32 v255, s5, 9
	v_cmp_gt_u32_e64 s[4:5], v15, v7
	v_or_b32_e32 v15, 19, v12
	v_cmp_gt_u32_e64 s[54:55], v15, v7
	v_writelane_b32 v255, s4, 10
	v_add_u32_e32 v223, v14, v11
	v_add_u32_e32 v224, v14, v3
	v_writelane_b32 v255, s5, 11
	v_cmp_lt_u32_e64 s[4:5], v15, v7
	v_or_b32_e32 v15, 24, v12
	v_cmp_lt_u32_e64 s[56:57], v15, v7
	v_cmp_gt_u32_e64 s[58:59], v15, v7
	v_or_b32_e32 v15, 25, v12
	v_cmp_lt_u32_e64 s[60:61], v15, v7
	v_cmp_gt_u32_e64 s[62:63], v15, v7
	v_or_b32_e32 v15, 26, v12
	v_or_b32_e32 v12, 27, v12
	v_cmp_lt_u32_e64 s[68:69], v12, v7
	v_cmp_gt_u32_e64 s[70:71], v12, v7
	v_lshlrev_b32_e32 v12, 5, v4
	v_and_b32_e32 v12, 0x180, v12
	v_lshl_or_b32 v6, v6, 9, v12
	v_cmp_lt_u32_e64 s[64:65], v15, v7
	v_cmp_gt_u32_e64 s[66:67], v15, v7
	v_add_u32_e32 v7, s75, v13
	v_or_b32_e32 v12, 0x800, v6
	v_xor_b32_e32 v4, v5, v4
	v_writelane_b32 v255, s4, 12
	v_add_u32_e32 v195, v7, v6
	v_add_u32_e32 v197, v12, v7
	v_add_u32_e32 v7, s83, v13
	v_lshlrev_b32_e32 v4, 4, v4
	v_or_b32_e32 v5, 24, v5
	v_writelane_b32 v255, s5, 13
	v_add_u32_e32 v199, v7, v6
	v_add_u32_e32 v201, v7, v12
	v_xor_b32_e32 v6, 16, v193
	v_xor_b32_e32 v7, 32, v193
	v_xor_b32_e32 v12, 48, v193
	v_xor_b32_e32 v13, 64, v193
	v_xor_b32_e32 v15, 0x50, v193
	v_and_b32_e32 v4, 0x70, v4
	v_lshl_add_u32 v19, v5, 7, s75
	v_or_b32_e32 v206, s3, v5
	v_mov_b32_e32 v5, 0x800
	s_add_i32 s4, s22, 0x7f8
	v_add_u32_e32 v196, 64, v195
	v_add_u32_e32 v198, 64, v197
	v_add_u32_e32 v200, 64, v199
	v_add_u32_e32 v202, 64, v201
	v_lshl_or_b32 v207, v9, 4, v5
	v_writelane_b32 v255, s4, 14
	s_add_i32 s22, s75, 0x2000
	v_add_u32_e32 v210, v194, v6
	v_add_u32_e32 v211, v194, v7
	v_add_u32_e32 v212, v194, v12
	v_add_u32_e32 v213, v194, v13
	v_add_u32_e32 v214, v194, v15
	v_add_u32_e32 v217, v18, v4
	v_add_u32_e32 v218, v20, v4
	v_add_u32_e32 v219, v21, v4
	v_add_u32_e32 v220, v19, v4
	v_mov_b32_e32 v226, 0xff800000
	s_mov_b32 s53, 0
	v_bfe_u32 v246, v0, 3, 3
	v_and_b32_e32 v251, 7, v0
	v_xor_b32_e32 v247, v251, v246
	v_lshlrev_b32_e32 v247, 4, v247
	v_add_u32_e32 v247, 0x800, v247
	v_add_u32_e32 v248, 0x800, v247
	v_add_u32_e32 v249, s3, v246
	v_add_u32_e32 v249, 32, v249
	s_cmp_eq_u32 s3, 0
	s_cselect_b32 s4, 0, 0x80
	s_add_i32 s4, s4, s3
	v_add_u32_e32 v250, s4, v246
	v_bfe_u32 v253, v0, 5, 1
	v_bfe_u32 v252, v0, 2, 2
	v_lshl_or_b32 v252, v253, 2, v252
	v_lshlrev_b32_e32 v252, 4, v252
	v_xor_b32_e32 v195, v252, v195
	v_xor_b32_e32 v196, v252, v196
	v_xor_b32_e32 v197, v252, v197
	v_xor_b32_e32 v198, v252, v198
	v_xor_b32_e32 v199, v252, v199
	v_xor_b32_e32 v200, v252, v200
	v_xor_b32_e32 v201, v252, v201
	v_xor_b32_e32 v202, v252, v202
	s_branch .LBB0_431
